# baseline (speedup 1.0000x reference)
.LBB1_115:
	s_or_b64 exec, exec, s[0:1]
	s_mov_b64 s[100:101], s[4:5]

.LBB1_120:
	s_or_b64 exec, exec, s[0:1]
	s_and_b64 vcc, exec, s[100:101]
	s_cbranch_vccnz .Lgw_cvt_skip
	v_cvt_f16_f32_e32 v98, v102
	v_cvt_pk_f16_f32 v103, v180, v181
	v_cvt_f16_f32_e32 v108, v189
	v_cvt_pk_f16_f32 v106, v182, v183
	v_pack_b32_f16 v104, v98, v103
	v_cvt_f16_f32_e32 v98, v188
	v_alignbit_b32 v105, v106, v103, 16
	v_cvt_pk_f16_f32 v103, v184, v185
	v_alignbit_b32 v106, v103, v106, 16
	v_alignbit_b32 v107, v98, v103, 16
	v_cvt_pk_f16_f32 v98, v186, v187
	v_pack_b32_f16 v110, v108, v98
	v_cvt_f16_f32_e32 v108, v109
	v_cvt_pk_f16_f32 v103, v190, v191
	v_alignbit_b32 v111, v103, v98, 16
	v_cvt_pk_f16_f32 v98, v192, v193
	v_lshl_add_u64 v[100:101], v[100:101], 4, s[66:67]
	v_alignbit_b32 v112, v98, v103, 16
	v_alignbit_b32 v113, v108, v98, 16
	global_store_dwordx4 v[100:101], v[104:107], off
	global_store_dwordx4 v[100:101], v[110:113], off offset:16
.Lgw_cvt_skip:
	s_cmp_eq_u32 s27, 32
	s_cbranch_scc1 .LBB1_122
	v_mov_b32_e32 v118, v194
	v_mov_b32_e32 v100, v195
	s_mov_b32 s30, s27
	s_branch .LBB1_29

	.amdhsa_kernel _Z9k_persist11PersistArgs
		.amdhsa_group_segment_fixed_size 0
		.amdhsa_private_segment_fixed_size 0
		.amdhsa_kernarg_size 192
		.amdhsa_user_sgpr_count 2
		.amdhsa_user_sgpr_dispatch_ptr 0
		.amdhsa_user_sgpr_queue_ptr 0
		.amdhsa_user_sgpr_kernarg_segment_ptr 1
		.amdhsa_user_sgpr_dispatch_id 0
		.amdhsa_user_sgpr_kernarg_preload_length 0
		.amdhsa_user_sgpr_kernarg_preload_offset 0
		.amdhsa_user_sgpr_private_segment_size 0
		.amdhsa_uses_dynamic_stack 0
		.amdhsa_enable_private_segment 0
		.amdhsa_system_sgpr_workgroup_id_x 1
		.amdhsa_system_sgpr_workgroup_id_y 0
		.amdhsa_system_sgpr_workgroup_id_z 0
		.amdhsa_system_sgpr_workgroup_info 0
		.amdhsa_system_vgpr_workitem_id 0
		.amdhsa_next_free_vgpr 241
		.amdhsa_next_free_sgpr 102
		.amdhsa_accum_offset 244
		.amdhsa_reserve_vcc 1
		.amdhsa_float_round_mode_32 0
		.amdhsa_float_round_mode_16_64 0
		.amdhsa_float_denorm_mode_32 3
		.amdhsa_float_denorm_mode_16_64 3
		.amdhsa_dx10_clamp 1
		.amdhsa_ieee_mode 1
		.amdhsa_fp16_overflow 0
		.amdhsa_tg_split 0
		.amdhsa_exception_fp_ieee_invalid_op 0
		.amdhsa_exception_fp_denorm_src 0
		.amdhsa_exception_fp_ieee_div_zero 0
		.amdhsa_exception_fp_ieee_overflow 0
		.amdhsa_exception_fp_ieee_underflow 0
		.amdhsa_exception_fp_ieee_inexact 0
		.amdhsa_exception_int_div_zero 0
	.end_amdhsa_kernel

amdhsa.kernels:
  - .agpr_count:     0
    .args:
      - .offset:         0
        .size:           200
        .value_kind:     by_value
    .group_segment_fixed_size: 4224
    .kernarg_segment_align: 8
    .kernarg_segment_size: 200
    .language:       OpenCL C
    .language_version:
      - 2
      - 0
    .max_flat_workgroup_size: 256
    .name:           _Z10k_prep_all8PrepArgs
    .private_segment_fixed_size: 0
    .sgpr_count:     74
    .sgpr_spill_count: 0
    .symbol:         _Z10k_prep_all8PrepArgs.kd
    .uniform_work_group_size: 1
    .uses_dynamic_stack: false
    .vgpr_count:     27
    .vgpr_spill_count: 0
    .wavefront_size: 64
  - .agpr_count:     0
    .args:
      - .offset:         0
        .size:           192
        .value_kind:     by_value
    .group_segment_fixed_size: 0
    .kernarg_segment_align: 8
    .kernarg_segment_size: 192
    .language:       OpenCL C
    .language_version:
      - 2
      - 0
    .max_flat_workgroup_size: 512
    .name:           _Z9k_persist11PersistArgs
    .private_segment_fixed_size: 0
    .sgpr_count:     108
    .sgpr_spill_count: 32
    .symbol:         _Z9k_persist11PersistArgs.kd
    .uniform_work_group_size: 1
    .uses_dynamic_stack: false
    .vgpr_count:     241
    .vgpr_spill_count: 0
    .wavefront_size: 64
  - .agpr_count:     0
    .args:
      - .actual_access:  read_only
        .address_space:  global
        .offset:         0
        .size:           8
        .value_kind:     global_buffer
      - .actual_access:  write_only
        .address_space:  global
        .offset:         8
        .size:           8
        .value_kind:     global_buffer
    .group_segment_fixed_size: 32
    .kernarg_segment_align: 8
    .kernarg_segment_size: 16
    .language:       OpenCL C
    .language_version:
      - 2
      - 0
    .max_flat_workgroup_size: 256
    .name:           _Z11k_lse_finalPKDF16_Pf
    .private_segment_fixed_size: 0
    .sgpr_count:     20
    .sgpr_spill_count: 0
    .symbol:         _Z11k_lse_finalPKDF16_Pf.kd
    .uniform_work_group_size: 1
    .uses_dynamic_stack: false
    .vgpr_count:     148
    .vgpr_spill_count: 0
    .wavefront_size: 64
  - .agpr_count:     0
    .args:
      - .address_space:  global
        .offset:         0
        .size:           8
        .value_kind:     global_buffer
      - .address_space:  global
        .offset:         8
        .size:           8
        .value_kind:     global_buffer
      - .actual_access:  write_only
        .address_space:  global
        .offset:         16
        .size:           8
        .value_kind:     global_buffer
      - .actual_access:  read_only
        .address_space:  global
        .offset:         24
        .size:           8
        .value_kind:     global_buffer
      - .actual_access:  read_only
        .address_space:  global
        .offset:         32
        .size:           8
        .value_kind:     global_buffer
      - .actual_access:  read_only
        .address_space:  global
        .offset:         40
        .size:           8
        .value_kind:     global_buffer
      - .offset:         48
        .size:           4
        .value_kind:     by_value
      - .offset:         52
        .size:           4
        .value_kind:     by_value
      - .actual_access:  read_only
        .address_space:  global
        .offset:         56
        .size:           8
        .value_kind:     global_buffer
      - .actual_access:  read_only
        .address_space:  global
        .offset:         64
        .size:           8
        .value_kind:     global_buffer
      - .actual_access:  read_only
        .address_space:  global
        .offset:         72
        .size:           8
        .value_kind:     global_buffer
    .group_segment_fixed_size: 0
    .kernarg_segment_align: 8
    .kernarg_segment_size: 80
    .language:       OpenCL C
    .language_version:
      - 2
      - 0
    .max_flat_workgroup_size: 512
    .name:           _Z6k_gemmILi8ELi512ELi0ELb0ELi0EEvPKDF16_S1_PfPDF16_S3_PKfiiS1_S1_S3_
    .private_segment_fixed_size: 0
    .sgpr_count:     32
    .sgpr_spill_count: 0
    .symbol:         _Z6k_gemmILi8ELi512ELi0ELb0ELi0EEvPKDF16_S1_PfPDF16_S3_PKfiiS1_S1_S3_.kd
    .uniform_work_group_size: 1
    .uses_dynamic_stack: false
    .vgpr_count:     246
    .vgpr_spill_count: 0
    .wavefront_size: 64
  - .agpr_count:     0
    .args:
      - .address_space:  global
        .offset:         0
        .size:           8
        .value_kind:     global_buffer
      - .address_space:  global
        .offset:         8
        .size:           8
        .value_kind:     global_buffer
      - .actual_access:  read_only
        .address_space:  global
        .offset:         16
        .size:           8
        .value_kind:     global_buffer
      - .actual_access:  write_only
        .address_space:  global
        .offset:         24
        .size:           8
        .value_kind:     global_buffer
      - .actual_access:  read_only
        .address_space:  global
        .offset:         32
        .size:           8
        .value_kind:     global_buffer
      - .actual_access:  read_only
        .address_space:  global
        .offset:         40
        .size:           8
        .value_kind:     global_buffer
      - .offset:         48
        .size:           4
        .value_kind:     by_value
      - .offset:         52
        .size:           4
        .value_kind:     by_value
      - .actual_access:  read_only
        .address_space:  global
        .offset:         56
        .size:           8
        .value_kind:     global_buffer
      - .actual_access:  read_only
        .address_space:  global
        .offset:         64
        .size:           8
        .value_kind:     global_buffer
      - .actual_access:  read_only
        .address_space:  global
        .offset:         72
        .size:           8
        .value_kind:     global_buffer
    .group_segment_fixed_size: 0
    .kernarg_segment_align: 8
    .kernarg_segment_size: 80
    .language:       OpenCL C
    .language_version:
      - 2
      - 0
    .max_flat_workgroup_size: 512
    .name:           _Z6k_gemmILi16ELi1024ELi0ELb0ELi3EEvPKDF16_S1_PfPDF16_S3_PKfiiS1_S1_S3_
    .private_segment_fixed_size: 0
    .sgpr_count:     36
    .sgpr_spill_count: 0
    .symbol:         _Z6k_gemmILi16ELi1024ELi0ELb0ELi3EEvPKDF16_S1_PfPDF16_S3_PKfiiS1_S1_S3_.kd
    .uniform_work_group_size: 1
    .uses_dynamic_stack: false
    .vgpr_count:     246
    .vgpr_spill_count: 0
    .wavefront_size: 64
  - .agpr_count:     0
    .args:
      - .address_space:  global
        .offset:         0
        .size:           8
        .value_kind:     global_buffer
      - .address_space:  global
        .offset:         8
        .size:           8
        .value_kind:     global_buffer
      - .actual_access:  read_only
        .address_space:  global
        .offset:         16
        .size:           8
        .value_kind:     global_buffer
      - .actual_access:  write_only
        .address_space:  global
        .offset:         24
        .size:           8
        .value_kind:     global_buffer
      - .actual_access:  write_only
        .address_space:  global
        .offset:         32
        .size:           8
        .value_kind:     global_buffer
      - .actual_access:  read_only
        .address_space:  global
        .offset:         40
        .size:           8
        .value_kind:     global_buffer
      - .offset:         48
        .size:           4
        .value_kind:     by_value
      - .offset:         52
        .size:           4
        .value_kind:     by_value
      - .address_space:  global
        .offset:         56
        .size:           8
        .value_kind:     global_buffer
      - .address_space:  global
        .offset:         64
        .size:           8
        .value_kind:     global_buffer
      - .actual_access:  write_only
        .address_space:  global
        .offset:         72
        .size:           8
        .value_kind:     global_buffer
    .group_segment_fixed_size: 0
    .kernarg_segment_align: 8
    .kernarg_segment_size: 80
    .language:       OpenCL C
    .language_version:
      - 2
      - 0
    .max_flat_workgroup_size: 512
    .name:           _Z6k_gemmILi48ELi2048ELi1ELb1ELi12EEvPKDF16_S1_PfPDF16_S3_PKfiiS1_S1_S3_
    .private_segment_fixed_size: 0
    .sgpr_count:     26
    .sgpr_spill_count: 0
    .symbol:         _Z6k_gemmILi48ELi2048ELi1ELb1ELi12EEvPKDF16_S1_PfPDF16_S3_PKfiiS1_S1_S3_.kd
    .uniform_work_group_size: 1
    .uses_dynamic_stack: false
    .vgpr_count:     242
    .vgpr_spill_count: 0
    .wavefront_size: 64
